# gate/up GEMM epilogue: the +1 of (clamp(up)+1) folded into the up-bias once per unit (clamp bounds -6..8), 32 packed adds per wave-unit removed
# speedup vs baseline: 1.0024x; 1.0024x over previous
; #define PG8_STAGE(bufoff, gbase, voff) do { _Pragma("unroll") for (int _i = 0; _i < 2; ++_i) \
;         __builtin_amdgcn_raw_ptr_buffer_load_lds(rsrc, (LAS void*)(lds + (bufoff) + ldsw + _i * 8192), 16, (int)(voff)[_i], (int)(gbase), 0, 0); } while (0)
; #define PG8_STAGE_A(bufoff, h, goff) do { if constexpr (GATHER) { PG8_STAGE(bufoff, goff, vG[h]); } else { PG8_STAGE(bufoff, (goff) + (h) * hstep, voffA); } } while (0)
; #define PG8_WAIT_V(n) asm volatile("s_waitcnt vmcnt(" #n ")" ::: "memory")
; #define PG8_BAR __builtin_amdgcn_s_barrier()
;     ...
;     if constexpr (SP2) {
;         PG8_STAGE(PG8_SB(0, 0), cB, voffB); PG8_STAGE(PG8_SB(0, 1), cB + hstep, voffB); PG8_STAGE_A(PG8_SA(0, 0), 0, cA); PG8_STAGE_A(PG8_SA(0, 1), 1, cA);
;         if (wr == 1) PG8_BAR;
;         PG8_WAIT_V(2); PG8_BAR;
;         PG8_STAGE(PG8_SB(1, 0), cB + kstep, voffB); PG8_STAGE_A(PG8_SA(1, 0), 0, cA + kstep); PG8_STAGE(PG8_SB(1, 1), cB + hstep + kstep, voffB);
;         PG8_WAIT_V(6); PG8_BAR;
;     __device__ __forceinline__ void operator()(const f32x4 (&acc)[2][2][4][2], const Unit& u, int wr, int wc, int fr, int fq) const {
;     ...
;                 for (int n = 0; n < 2; ++n) { const f32x4 g4 = acc[ai][0][m][n] * WSCALE_INV + bgv[n], u4 = acc[ai][1][m][n] * WSCALE_INV + buv[n];
; #pragma unroll
;                     for (int e = 0; e < 4; e += 2) {
;                         f32x2 g = {fminf(g4[e], 7.0f), fminf(g4[e + 1], 7.0f)}; const f32x2 up = {fminf(fmaxf(u4[e], -7.0f), 7.0f), fminf(fmaxf(u4[e + 1], -7.0f), 7.0f)};
;                         const f32x2 z = g * (-2.4554669595930157f); f32x2 ex; ex.x = __builtin_amdgcn_exp2f(z.x); ex.y = __builtin_amdgcn_exp2f(z.y);
;                         const f32x2 den = ex + 1.0f; f32x2 sg; sg.x = __builtin_amdgcn_rcpf(den.x); sg.y = __builtin_amdgcn_rcpf(den.y);
;                         const f32x2 r = (up + 1.0f) * g * sg; o[4 * n + e] = r.x; o[4 * n + e + 1] = r.y; } }
.LBB0_1227:
	s_add_i32 s39, s21, 0x18000
	s_add_i32 s1, s64, 0x80
	s_mov_b32 m0, s39
	s_add_i32 s40, s21, 0x1a000
	s_waitcnt vmcnt(2)
	s_barrier
	buffer_load_dwordx4 v192, s[4:7], s1 offen lds
	s_mov_b32 m0, s40
	s_add_i32 s41, s21, 0x8000
	buffer_load_dwordx4 v193, s[4:7], s1 offen lds
	s_mov_b32 s1, 0x70e00080
	s_mov_b32 m0, s41
	s_add_i32 s42, s21, 0xa000
	buffer_load_dwordx4 v196, s[4:7], s1 offen lds
	s_mov_b32 m0, s42
	s_add_i32 s43, s21, 0x1c000
	buffer_load_dwordx4 v194, s[4:7], s1 offen lds
	s_add_i32 s1, s64, 0x40080
	s_mov_b32 m0, s43
	s_add_i32 s44, s21, 0x1e000
	buffer_load_dwordx4 v192, s[4:7], s1 offen lds
	s_mov_b32 m0, s44
	v_lshrrev_b32_e32 v1, 3, v0
	buffer_load_dwordx4 v193, s[4:7], s1 offen lds
	v_and_b32_e32 v3, 7, v0
	v_lshlrev_b32_e32 v0, 4, v0
	v_and_b32_e32 v0, 0x80, v0
	s_and_b32 s1, s3, 3
	v_and_b32_e32 v2, 6, v1
	v_lshl_or_b32 v0, v3, 8, v0
	v_bitop3_b32 v1, v1, v3, 6 bitop3:0x6c
	s_lshl_b32 s4, s0, 13
	s_lshl_b32 s16, s1, 12
	v_lshl_or_b32 v1, v1, 4, v0
	v_or_b32_e32 v4, s4, v1
	v_or_b32_e32 v198, s16, v1
	v_bitop3_b32 v1, v2, v3, 1 bitop3:0x36
	v_lshl_or_b32 v0, v1, 4, v0
	v_or_b32_e32 v1, s4, v0
	s_lshl_b32 s4, s3, 9
	s_add_i32 s45, s4, 0
	s_add_i32 s46, s21, 0xc000
	s_cmpk_lt_u32 s2, 0x100
	v_or_b32_e32 v199, s16, v0
	s_cselect_b64 s[16:17], -1, 0
	s_lshl_b32 s47, s1, 5
	s_lshl_b32 s1, s1, 7
	s_add_i32 s48, s1, 0
	v_readlane_b32 s52, v254, 2
	s_add_i32 s48, s48, 0x25000
	s_lshl_b32 s49, s0, 6
	s_add_i32 s50, s21, 0xe000
	v_readlane_b32 s54, v254, 4
	v_readlane_b32 s55, v254, 5
	s_add_u32 s51, s54, 0x5fe00000
	s_waitcnt vmcnt(6)
	v_readlane_b32 s53, v254, 3
	s_addc_u32 s52, s55, 0
	s_add_i32 s0, 0, 0x10000
	s_lshl_b32 s53, s3, 13
	v_add_u32_e32 v200, s0, v198
	v_add_u32_e32 v201, s0, v199
	s_add_i32 s0, 0, 0x14000
	s_add_i32 s53, s53, 0x4edf4000
	v_add_u32_e32 v202, s0, v198
	v_add_u32_e32 v203, s0, v199
	v_add_u32_e32 v204, 0, v4
	v_add_u32_e32 v205, 0, v1
	s_mov_b32 s18, 0x3b000000
	s_mov_b32 s54, 0xc0c00000
	s_mov_b32 s20, 0xc01d265f
	s_mov_b32 s55, 0x48000
	s_mov_b32 s56, 0x50000
	v_mov_b32_e32 v206, 0x41000000
	s_barrier
	s_branch .LBB0_1230

; #define LAS __attribute__((address_space(3)))
; DI unsigned pk4f8(float a, float b, float c, float d) { int p = __builtin_amdgcn_cvt_pk_fp8_f32(a, b, 0, false); p = __builtin_amdgcn_cvt_pk_fp8_f32(c, d, p, true); return (unsigned)p; }
;     __device__ __forceinline__ void operator()(const f32x4 (&acc)[2][2][4][2], const Unit& u, int wr, int wc, int fr, int fq) const {
;         unsigned char* base = (unsigned char*)u.O; const int acol = u.a1 * 128 + wc * 32 + 8 * fq;
;         const LAS float* bt = (const LAS float*)((LAS unsigned char*)lds_raw + LDS_CTL_OFF + 4096 + u.buf * 1024) + wc * 32 + 8 * fq;
;         const int row0 = wr * 64 + fr;
;         f32x4 bgv[2], buv[2];
; #pragma unroll
;         for (int n = 0; n < 2; ++n) { bgv[n] = *(const LAS f32x4*)(bt + 4 * n); buv[n] = *(const LAS f32x4*)(bt + 128 + 4 * n); }
; #pragma unroll
;         for (int ai = 0; ai < 2; ++ai)
; #pragma unroll
;             for (int m = 0; m < 4; ++m) {
;                 float o[8];
; #pragma unroll
;                 for (int n = 0; n < 2; ++n) { const f32x4 g4 = acc[ai][0][m][n] * WSCALE_INV + bgv[n], u4 = acc[ai][1][m][n] * WSCALE_INV + buv[n];
; #pragma unroll
;                     for (int e = 0; e < 4; e += 2) {
;                         f32x2 g = {fminf(g4[e], 7.0f), fminf(g4[e + 1], 7.0f)}; const f32x2 up = {fminf(fmaxf(u4[e], -7.0f), 7.0f), fminf(fmaxf(u4[e + 1], -7.0f), 7.0f)};
;                         const f32x2 z = g * (-2.4554669595930157f); f32x2 ex; ex.x = __builtin_amdgcn_exp2f(z.x); ex.y = __builtin_amdgcn_exp2f(z.y);
;                         const f32x2 den = ex + 1.0f; f32x2 sg; sg.x = __builtin_amdgcn_rcpf(den.x); sg.y = __builtin_amdgcn_rcpf(den.y);
;                         const f32x2 r = (up + 1.0f) * g * sg; o[4 * n + e] = r.x; o[4 * n + e + 1] = r.y; } }
;                 u32x2 w; w.x = pk4f8(o[0], o[1], o[2], o[3]); w.y = pk4f8(o[4], o[5], o[6], o[7]);
;                 *(u32x2*)(base + (size_t)(row0 + ai * HALF + m * 16) * 2048 + acol) = w; __builtin_amdgcn_sched_barrier(0); }
.LBB0_1254:
	v_mbcnt_lo_u32_b32 v17, -1, 0
	v_mbcnt_hi_u32_b32 v17, -1, v17
	s_lshl_b32 s2, s65, 10
	s_and_b32 s2, s2, 0x400
	v_ashrrev_i32_e32 v0, 1, v17
	v_and_b32_e32 v16, -8, v0
	s_add_i32 s2, s48, s2
	v_lshl_add_u32 v0, v16, 2, s2
	ds_read_b128 v[12:15], v0
	ds_read_b128 v[4:7], v0 offset:16
	ds_read_b128 v[8:11], v0 offset:512
	ds_read_b128 v[0:3], v0 offset:528
	s_lshl_b32 s2, s63, 7
	s_waitcnt lgkmcnt(3)
	v_pk_fma_f32 v[22:23], v[188:189], s[18:19], v[12:13] op_sel_hi:[1,0,1]
	s_or_b32 s2, s2, s47
	v_min_f32_e32 v22, 0x40e00000, v22
	v_min_f32_e32 v23, 0x40e00000, v23
	v_pk_mul_f32 v[26:27], v[22:23], s[20:21] op_sel_hi:[1,0]
	v_add_u32_e32 v16, s2, v16
	v_exp_f32_e32 v26, v26
	v_exp_f32_e32 v27, v27
	v_and_or_b32 v20, v17, 15, s49
	v_ashrrev_i32_e32 v17, 31, v16
	v_lshl_add_u64 v[18:19], s[24:25], 0, v[16:17]
	v_pk_fma_f32 v[16:17], v[190:191], s[18:19], v[14:15] op_sel_hi:[1,0,1]
	v_pk_add_f32 v[26:27], v[26:27], 1.0 op_sel_hi:[1,0]
	v_min_f32_e32 v16, 0x40e00000, v16
	v_min_f32_e32 v17, 0x40e00000, v17
	v_pk_mul_f32 v[30:31], v[16:17], s[20:21] op_sel_hi:[1,0]
	s_waitcnt lgkmcnt(1)
	v_pk_add_f32 v[8:9], v[8:9], 1.0 op_sel_hi:[1,0]
	v_pk_add_f32 v[10:11], v[10:11], 1.0 op_sel_hi:[1,0]
	v_pk_fma_f32 v[28:29], v[184:185], s[18:19], v[8:9] op_sel_hi:[1,0,1]
	v_rcp_f32_e32 v26, v26
	v_rcp_f32_e32 v27, v27
	v_exp_f32_e32 v30, v30
	v_exp_f32_e32 v31, v31
	v_med3_f32 v28, v28, s54, v206
	v_med3_f32 v29, v29, s54, v206
	v_pk_fma_f32 v[24:25], v[186:187], s[18:19], v[10:11] op_sel_hi:[1,0,1]
	v_pk_mul_f32 v[22:23], v[22:23], v[28:29]
	v_med3_f32 v24, v24, s54, v206
	v_pk_mul_f32 v[22:23], v[22:23], v[26:27]
	v_pk_add_f32 v[26:27], v[30:31], 1.0 op_sel_hi:[1,0]
	v_med3_f32 v25, v25, s54, v206
	v_rcp_f32_e32 v26, v26
	v_rcp_f32_e32 v27, v27
	s_waitcnt lgkmcnt(0)
	v_pk_add_f32 v[0:1], v[0:1], 1.0 op_sel_hi:[1,0]
	v_pk_add_f32 v[2:3], v[2:3], 1.0 op_sel_hi:[1,0]
	v_pk_fma_f32 v[32:33], v[176:177], s[18:19], v[0:1] op_sel_hi:[1,0,1]
	v_pk_mul_f32 v[16:17], v[16:17], v[24:25]
	v_pk_fma_f32 v[24:25], v[182:183], s[18:19], v[6:7] op_sel_hi:[1,0,1]
	v_pk_mul_f32 v[16:17], v[16:17], v[26:27]
	v_pk_fma_f32 v[26:27], v[180:181], s[18:19], v[4:5] op_sel_hi:[1,0,1]
	v_med3_f32 v32, v32, s54, v206
	v_min_f32_e32 v26, 0x40e00000, v26
	v_min_f32_e32 v27, 0x40e00000, v27
	v_pk_mul_f32 v[30:31], v[26:27], s[20:21] op_sel_hi:[1,0]
	v_med3_f32 v33, v33, s54, v206
	v_exp_f32_e32 v30, v30
	v_exp_f32_e32 v31, v31
	v_min_f32_e32 v24, 0x40e00000, v24
	v_min_f32_e32 v25, 0x40e00000, v25
	v_pk_add_f32 v[30:31], v[30:31], 1.0 op_sel_hi:[1,0]
	v_pk_mul_f32 v[26:27], v[26:27], v[32:33]
	v_pk_mul_f32 v[32:33], v[24:25], s[20:21] op_sel_hi:[1,0]
	v_rcp_f32_e32 v30, v30
	v_rcp_f32_e32 v31, v31
	v_exp_f32_e32 v32, v32
	v_exp_f32_e32 v33, v33
	v_pk_fma_f32 v[28:29], v[178:179], s[18:19], v[2:3] op_sel_hi:[1,0,1]
	v_pk_mul_f32 v[26:27], v[26:27], v[30:31]
	v_med3_f32 v28, v28, s54, v206
	v_pk_add_f32 v[30:31], v[32:33], 1.0 op_sel_hi:[1,0]
	v_rcp_f32_e32 v30, v30
	v_rcp_f32_e32 v31, v31
	v_med3_f32 v29, v29, s54, v206
	v_cvt_pk_fp8_f32 v32, v22, v23
	v_cvt_pk_fp8_f32 v33, v26, v27
	v_ashrrev_i32_e32 v21, 31, v20
	v_pk_mul_f32 v[22:23], v[24:25], v[28:29]
	v_cvt_pk_fp8_f32 v32, v16, v17 op_sel:[0,0,1]
	v_pk_mul_f32 v[22:23], v[22:23], v[30:31]
	v_lshlrev_b64 v[16:17], 11, v[20:21]
	v_cvt_pk_fp8_f32 v33, v22, v23 op_sel:[0,0,1]
	v_lshl_add_u64 v[16:17], v[18:19], 0, v[16:17]
	global_store_dwordx2 v[16:17], v[32:33], off
	v_pk_fma_f32 v[24:25], v[172:173], s[18:19], v[12:13] op_sel_hi:[1,0,1]
	v_pk_fma_f32 v[22:23], v[174:175], s[18:19], v[14:15] op_sel_hi:[1,0,1]
	v_min_f32_e32 v24, 0x40e00000, v24
	v_min_f32_e32 v25, 0x40e00000, v25
	v_pk_mul_f32 v[28:29], v[24:25], s[20:21] op_sel_hi:[1,0]
	v_min_f32_e32 v22, 0x40e00000, v22
	v_exp_f32_e32 v28, v28
	v_exp_f32_e32 v29, v29
	v_min_f32_e32 v23, 0x40e00000, v23
	v_pk_mul_f32 v[32:33], v[22:23], s[20:21] op_sel_hi:[1,0]
	v_pk_fma_f32 v[30:31], v[168:169], s[18:19], v[8:9] op_sel_hi:[1,0,1]
	v_pk_add_f32 v[28:29], v[28:29], 1.0 op_sel_hi:[1,0]
	v_exp_f32_e32 v32, v32
	v_rcp_f32_e32 v28, v28
	v_rcp_f32_e32 v29, v29
	v_exp_f32_e32 v33, v33
	v_med3_f32 v30, v30, s54, v206
	v_med3_f32 v31, v31, s54, v206
	v_pk_fma_f32 v[26:27], v[170:171], s[18:19], v[10:11] op_sel_hi:[1,0,1]
	v_pk_mul_f32 v[24:25], v[24:25], v[30:31]
	v_med3_f32 v26, v26, s54, v206
	v_pk_mul_f32 v[24:25], v[24:25], v[28:29]
	v_pk_add_f32 v[28:29], v[32:33], 1.0 op_sel_hi:[1,0]
	v_med3_f32 v27, v27, s54, v206
	v_rcp_f32_e32 v28, v28
	v_rcp_f32_e32 v29, v29
	v_pk_fma_f32 v[34:35], v[160:161], s[18:19], v[0:1] op_sel_hi:[1,0,1]
	v_pk_mul_f32 v[22:23], v[22:23], v[26:27]
	v_pk_fma_f32 v[26:27], v[166:167], s[18:19], v[6:7] op_sel_hi:[1,0,1]
	v_pk_mul_f32 v[22:23], v[22:23], v[28:29]
	v_pk_fma_f32 v[28:29], v[164:165], s[18:19], v[4:5] op_sel_hi:[1,0,1]
	v_med3_f32 v34, v34, s54, v206
	v_min_f32_e32 v28, 0x40e00000, v28
	v_min_f32_e32 v29, 0x40e00000, v29
	v_pk_mul_f32 v[32:33], v[28:29], s[20:21] op_sel_hi:[1,0]
	v_med3_f32 v35, v35, s54, v206
	v_exp_f32_e32 v32, v32
	v_exp_f32_e32 v33, v33
	v_min_f32_e32 v26, 0x40e00000, v26
	v_min_f32_e32 v27, 0x40e00000, v27
	v_pk_add_f32 v[32:33], v[32:33], 1.0 op_sel_hi:[1,0]
	v_pk_mul_f32 v[28:29], v[28:29], v[34:35]
	v_pk_mul_f32 v[34:35], v[26:27], s[20:21] op_sel_hi:[1,0]
	v_rcp_f32_e32 v32, v32
	v_rcp_f32_e32 v33, v33
	v_exp_f32_e32 v34, v34
	v_exp_f32_e32 v35, v35
	v_pk_fma_f32 v[30:31], v[162:163], s[18:19], v[2:3] op_sel_hi:[1,0,1]
	v_pk_mul_f32 v[28:29], v[28:29], v[32:33]
	v_med3_f32 v30, v30, s54, v206
	v_pk_add_f32 v[32:33], v[34:35], 1.0 op_sel_hi:[1,0]
	v_rcp_f32_e32 v32, v32
	v_rcp_f32_e32 v33, v33
; #define LAS __attribute__((address_space(3)))
; DI unsigned pk4f8(float a, float b, float c, float d) { int p = __builtin_amdgcn_cvt_pk_fp8_f32(a, b, 0, false); p = __builtin_amdgcn_cvt_pk_fp8_f32(c, d, p, true); return (unsigned)p; }
;     __device__ __forceinline__ void operator()(const f32x4 (&acc)[2][2][4][2], const Unit& u, int wr, int wc, int fr, int fq) const {
;         unsigned char* base = (unsigned char*)u.O; const int acol = u.a1 * 128 + wc * 32 + 8 * fq;
;         const LAS float* bt = (const LAS float*)((LAS unsigned char*)lds_raw + LDS_CTL_OFF + 4096 + u.buf * 1024) + wc * 32 + 8 * fq;
;         const int row0 = wr * 64 + fr;
;         f32x4 bgv[2], buv[2];
; #pragma unroll
;         for (int n = 0; n < 2; ++n) { bgv[n] = *(const LAS f32x4*)(bt + 4 * n); buv[n] = *(const LAS f32x4*)(bt + 128 + 4 * n); }
; #pragma unroll
;         for (int ai = 0; ai < 2; ++ai)
; #pragma unroll
;             for (int m = 0; m < 4; ++m) {
;                 float o[8];
; #pragma unroll
;                 for (int n = 0; n < 2; ++n) { const f32x4 g4 = acc[ai][0][m][n] * WSCALE_INV + bgv[n], u4 = acc[ai][1][m][n] * WSCALE_INV + buv[n];
; #pragma unroll
;                     for (int e = 0; e < 4; e += 2) {
;                         f32x2 g = {fminf(g4[e], 7.0f), fminf(g4[e + 1], 7.0f)}; const f32x2 up = {fminf(fmaxf(u4[e], -7.0f), 7.0f), fminf(fmaxf(u4[e + 1], -7.0f), 7.0f)};
;                         const f32x2 z = g * (-2.4554669595930157f); f32x2 ex; ex.x = __builtin_amdgcn_exp2f(z.x); ex.y = __builtin_amdgcn_exp2f(z.y);
;                         const f32x2 den = ex + 1.0f; f32x2 sg; sg.x = __builtin_amdgcn_rcpf(den.x); sg.y = __builtin_amdgcn_rcpf(den.y);
;                         const f32x2 r = (up + 1.0f) * g * sg; o[4 * n + e] = r.x; o[4 * n + e + 1] = r.y; } }
;                 u32x2 w; w.x = pk4f8(o[0], o[1], o[2], o[3]); w.y = pk4f8(o[4], o[5], o[6], o[7]);
;                 *(u32x2*)(base + (size_t)(row0 + ai * HALF + m * 16) * 2048 + acol) = w; __builtin_amdgcn_sched_barrier(0); }
	v_med3_f32 v31, v31, s54, v206
	v_cvt_pk_fp8_f32 v34, v24, v25
	v_cvt_pk_fp8_f32 v35, v28, v29
	v_cvt_pk_fp8_f32 v34, v22, v23 op_sel:[0,0,1]
	v_pk_mul_f32 v[24:25], v[26:27], v[30:31]
	v_or_b32_e32 v22, 16, v20
	v_pk_mul_f32 v[24:25], v[24:25], v[32:33]
	v_ashrrev_i32_e32 v23, 31, v22
	v_cvt_pk_fp8_f32 v35, v24, v25 op_sel:[0,0,1]
	v_lshlrev_b64 v[22:23], 11, v[22:23]
	v_lshl_add_u64 v[22:23], v[18:19], 0, v[22:23]
	global_store_dwordx2 v[22:23], v[34:35], off
	v_pk_fma_f32 v[24:25], v[156:157], s[18:19], v[12:13] op_sel_hi:[1,0,1]
	v_pk_fma_f32 v[22:23], v[158:159], s[18:19], v[14:15] op_sel_hi:[1,0,1]
	v_min_f32_e32 v24, 0x40e00000, v24
	v_min_f32_e32 v25, 0x40e00000, v25
	v_pk_mul_f32 v[28:29], v[24:25], s[20:21] op_sel_hi:[1,0]
	v_min_f32_e32 v22, 0x40e00000, v22
	v_exp_f32_e32 v28, v28
	v_exp_f32_e32 v29, v29
	v_min_f32_e32 v23, 0x40e00000, v23
	v_pk_mul_f32 v[32:33], v[22:23], s[20:21] op_sel_hi:[1,0]
	v_pk_fma_f32 v[30:31], v[152:153], s[18:19], v[8:9] op_sel_hi:[1,0,1]
	v_pk_add_f32 v[28:29], v[28:29], 1.0 op_sel_hi:[1,0]
	v_exp_f32_e32 v32, v32
	v_rcp_f32_e32 v28, v28
	v_rcp_f32_e32 v29, v29
	v_exp_f32_e32 v33, v33
	v_med3_f32 v30, v30, s54, v206
	v_med3_f32 v31, v31, s54, v206
	v_pk_fma_f32 v[26:27], v[154:155], s[18:19], v[10:11] op_sel_hi:[1,0,1]
	v_pk_mul_f32 v[24:25], v[24:25], v[30:31]
	v_med3_f32 v26, v26, s54, v206
	v_pk_mul_f32 v[24:25], v[24:25], v[28:29]
	v_pk_add_f32 v[28:29], v[32:33], 1.0 op_sel_hi:[1,0]
	v_med3_f32 v27, v27, s54, v206
	v_rcp_f32_e32 v28, v28
	v_rcp_f32_e32 v29, v29
	v_pk_fma_f32 v[34:35], v[144:145], s[18:19], v[0:1] op_sel_hi:[1,0,1]
	v_pk_mul_f32 v[22:23], v[22:23], v[26:27]
	v_pk_fma_f32 v[26:27], v[150:151], s[18:19], v[6:7] op_sel_hi:[1,0,1]
	v_pk_mul_f32 v[22:23], v[22:23], v[28:29]
	v_pk_fma_f32 v[28:29], v[148:149], s[18:19], v[4:5] op_sel_hi:[1,0,1]
	v_med3_f32 v34, v34, s54, v206
	v_min_f32_e32 v28, 0x40e00000, v28
	v_min_f32_e32 v29, 0x40e00000, v29
	v_pk_mul_f32 v[32:33], v[28:29], s[20:21] op_sel_hi:[1,0]
	v_med3_f32 v35, v35, s54, v206
	v_exp_f32_e32 v32, v32
	v_exp_f32_e32 v33, v33
	v_min_f32_e32 v26, 0x40e00000, v26
	v_min_f32_e32 v27, 0x40e00000, v27
	v_pk_add_f32 v[32:33], v[32:33], 1.0 op_sel_hi:[1,0]
	v_pk_mul_f32 v[28:29], v[28:29], v[34:35]
	v_pk_mul_f32 v[34:35], v[26:27], s[20:21] op_sel_hi:[1,0]
	v_rcp_f32_e32 v32, v32
	v_rcp_f32_e32 v33, v33
	v_exp_f32_e32 v34, v34
	v_exp_f32_e32 v35, v35
	v_pk_fma_f32 v[30:31], v[146:147], s[18:19], v[2:3] op_sel_hi:[1,0,1]
	v_pk_mul_f32 v[28:29], v[28:29], v[32:33]
	v_med3_f32 v30, v30, s54, v206
	v_pk_add_f32 v[32:33], v[34:35], 1.0 op_sel_hi:[1,0]
	v_rcp_f32_e32 v32, v32
	v_rcp_f32_e32 v33, v33
	v_med3_f32 v31, v31, s54, v206
	v_cvt_pk_fp8_f32 v34, v24, v25
	v_cvt_pk_fp8_f32 v35, v28, v29
	v_cvt_pk_fp8_f32 v34, v22, v23 op_sel:[0,0,1]
	v_pk_mul_f32 v[24:25], v[26:27], v[30:31]
	v_or_b32_e32 v22, 32, v20
	v_pk_mul_f32 v[24:25], v[24:25], v[32:33]
	v_ashrrev_i32_e32 v23, 31, v22
	v_cvt_pk_fp8_f32 v35, v24, v25 op_sel:[0,0,1]
	v_lshlrev_b64 v[22:23], 11, v[22:23]
	v_lshl_add_u64 v[22:23], v[18:19], 0, v[22:23]
	global_store_dwordx2 v[22:23], v[34:35], off
	v_pk_fma_f32 v[24:25], v[140:141], s[18:19], v[12:13] op_sel_hi:[1,0,1]
	v_pk_fma_f32 v[22:23], v[142:143], s[18:19], v[14:15] op_sel_hi:[1,0,1]
	v_min_f32_e32 v24, 0x40e00000, v24
	v_min_f32_e32 v25, 0x40e00000, v25
	v_pk_mul_f32 v[28:29], v[24:25], s[20:21] op_sel_hi:[1,0]
	v_min_f32_e32 v22, 0x40e00000, v22
	v_exp_f32_e32 v28, v28
	v_exp_f32_e32 v29, v29
	v_min_f32_e32 v23, 0x40e00000, v23
	v_pk_mul_f32 v[32:33], v[22:23], s[20:21] op_sel_hi:[1,0]
	v_pk_fma_f32 v[30:31], v[136:137], s[18:19], v[8:9] op_sel_hi:[1,0,1]
	v_pk_add_f32 v[28:29], v[28:29], 1.0 op_sel_hi:[1,0]
	v_exp_f32_e32 v32, v32
	v_rcp_f32_e32 v28, v28
	v_rcp_f32_e32 v29, v29
	v_exp_f32_e32 v33, v33
	v_med3_f32 v30, v30, s54, v206
	v_med3_f32 v31, v31, s54, v206
	v_pk_fma_f32 v[26:27], v[138:139], s[18:19], v[10:11] op_sel_hi:[1,0,1]
	v_pk_mul_f32 v[24:25], v[24:25], v[30:31]
	v_med3_f32 v26, v26, s54, v206
	v_pk_mul_f32 v[24:25], v[24:25], v[28:29]
	v_pk_add_f32 v[28:29], v[32:33], 1.0 op_sel_hi:[1,0]
	v_med3_f32 v27, v27, s54, v206
	v_rcp_f32_e32 v28, v28
	v_rcp_f32_e32 v29, v29
	v_pk_fma_f32 v[34:35], v[128:129], s[18:19], v[0:1] op_sel_hi:[1,0,1]
	v_pk_mul_f32 v[22:23], v[22:23], v[26:27]
	v_pk_fma_f32 v[26:27], v[134:135], s[18:19], v[6:7] op_sel_hi:[1,0,1]
	v_pk_mul_f32 v[22:23], v[22:23], v[28:29]
	v_pk_fma_f32 v[28:29], v[132:133], s[18:19], v[4:5] op_sel_hi:[1,0,1]
	v_med3_f32 v34, v34, s54, v206
	v_min_f32_e32 v28, 0x40e00000, v28
	v_min_f32_e32 v29, 0x40e00000, v29
	v_pk_mul_f32 v[32:33], v[28:29], s[20:21] op_sel_hi:[1,0]
	v_med3_f32 v35, v35, s54, v206
	v_exp_f32_e32 v32, v32
	v_exp_f32_e32 v33, v33
	v_min_f32_e32 v26, 0x40e00000, v26
	v_min_f32_e32 v27, 0x40e00000, v27
	v_pk_add_f32 v[32:33], v[32:33], 1.0 op_sel_hi:[1,0]
	v_pk_mul_f32 v[28:29], v[28:29], v[34:35]
	v_pk_mul_f32 v[34:35], v[26:27], s[20:21] op_sel_hi:[1,0]
	v_rcp_f32_e32 v32, v32
	v_rcp_f32_e32 v33, v33
	v_exp_f32_e32 v34, v34
	v_exp_f32_e32 v35, v35
	v_pk_fma_f32 v[30:31], v[130:131], s[18:19], v[2:3] op_sel_hi:[1,0,1]
	v_pk_mul_f32 v[28:29], v[28:29], v[32:33]
	v_med3_f32 v30, v30, s54, v206
	v_pk_add_f32 v[32:33], v[34:35], 1.0 op_sel_hi:[1,0]
	v_rcp_f32_e32 v32, v32
	v_rcp_f32_e32 v33, v33
	v_med3_f32 v31, v31, s54, v206
	v_cvt_pk_fp8_f32 v34, v24, v25
	v_cvt_pk_fp8_f32 v35, v28, v29
	v_or_b32_e32 v20, 48, v20
	v_pk_mul_f32 v[24:25], v[26:27], v[30:31]
	v_cvt_pk_fp8_f32 v34, v22, v23 op_sel:[0,0,1]
	v_pk_mul_f32 v[24:25], v[24:25], v[32:33]
	v_ashrrev_i32_e32 v21, 31, v20
	v_cvt_pk_fp8_f32 v35, v24, v25 op_sel:[0,0,1]
; #define LAS __attribute__((address_space(3)))
; DI unsigned pk4f8(float a, float b, float c, float d) { int p = __builtin_amdgcn_cvt_pk_fp8_f32(a, b, 0, false); p = __builtin_amdgcn_cvt_pk_fp8_f32(c, d, p, true); return (unsigned)p; }
;     __device__ __forceinline__ void operator()(const f32x4 (&acc)[2][2][4][2], const Unit& u, int wr, int wc, int fr, int fq) const {
;         unsigned char* base = (unsigned char*)u.O; const int acol = u.a1 * 128 + wc * 32 + 8 * fq;
;         const LAS float* bt = (const LAS float*)((LAS unsigned char*)lds_raw + LDS_CTL_OFF + 4096 + u.buf * 1024) + wc * 32 + 8 * fq;
;         const int row0 = wr * 64 + fr;
;         f32x4 bgv[2], buv[2];
; #pragma unroll
;         for (int n = 0; n < 2; ++n) { bgv[n] = *(const LAS f32x4*)(bt + 4 * n); buv[n] = *(const LAS f32x4*)(bt + 128 + 4 * n); }
; #pragma unroll
;         for (int ai = 0; ai < 2; ++ai)
; #pragma unroll
;             for (int m = 0; m < 4; ++m) {
;                 float o[8];
; #pragma unroll
;                 for (int n = 0; n < 2; ++n) { const f32x4 g4 = acc[ai][0][m][n] * WSCALE_INV + bgv[n], u4 = acc[ai][1][m][n] * WSCALE_INV + buv[n];
; #pragma unroll
;                     for (int e = 0; e < 4; e += 2) {
;                         f32x2 g = {fminf(g4[e], 7.0f), fminf(g4[e + 1], 7.0f)}; const f32x2 up = {fminf(fmaxf(u4[e], -7.0f), 7.0f), fminf(fmaxf(u4[e + 1], -7.0f), 7.0f)};
;                         const f32x2 z = g * (-2.4554669595930157f); f32x2 ex; ex.x = __builtin_amdgcn_exp2f(z.x); ex.y = __builtin_amdgcn_exp2f(z.y);
;                         const f32x2 den = ex + 1.0f; f32x2 sg; sg.x = __builtin_amdgcn_rcpf(den.x); sg.y = __builtin_amdgcn_rcpf(den.y);
;                         const f32x2 r = (up + 1.0f) * g * sg; o[4 * n + e] = r.x; o[4 * n + e + 1] = r.y; } }
;                 u32x2 w; w.x = pk4f8(o[0], o[1], o[2], o[3]); w.y = pk4f8(o[4], o[5], o[6], o[7]);
;                 *(u32x2*)(base + (size_t)(row0 + ai * HALF + m * 16) * 2048 + acol) = w; __builtin_amdgcn_sched_barrier(0); }
	v_lshlrev_b64 v[20:21], 11, v[20:21]
	v_lshl_add_u64 v[18:19], v[18:19], 0, v[20:21]
	global_store_dwordx2 v[18:19], v[34:35], off
	v_pk_fma_f32 v[20:21], v[124:125], s[18:19], v[12:13] op_sel_hi:[1,0,1]
	v_pk_fma_f32 v[18:19], v[126:127], s[18:19], v[14:15] op_sel_hi:[1,0,1]
	v_min_f32_e32 v20, 0x40e00000, v20
	v_min_f32_e32 v21, 0x40e00000, v21
	v_pk_mul_f32 v[24:25], v[20:21], s[20:21] op_sel_hi:[1,0]
	v_min_f32_e32 v18, 0x40e00000, v18
	v_exp_f32_e32 v24, v24
	v_exp_f32_e32 v25, v25
	v_min_f32_e32 v19, 0x40e00000, v19
	v_pk_mul_f32 v[28:29], v[18:19], s[20:21] op_sel_hi:[1,0]
	v_pk_fma_f32 v[26:27], v[120:121], s[18:19], v[8:9] op_sel_hi:[1,0,1]
	v_pk_add_f32 v[24:25], v[24:25], 1.0 op_sel_hi:[1,0]
	v_exp_f32_e32 v28, v28
	v_rcp_f32_e32 v24, v24
	v_rcp_f32_e32 v25, v25
	v_exp_f32_e32 v29, v29
	v_med3_f32 v26, v26, s54, v206
	v_med3_f32 v27, v27, s54, v206
	v_pk_fma_f32 v[22:23], v[122:123], s[18:19], v[10:11] op_sel_hi:[1,0,1]
	v_pk_mul_f32 v[20:21], v[20:21], v[26:27]
	v_med3_f32 v22, v22, s54, v206
	v_pk_mul_f32 v[20:21], v[20:21], v[24:25]
	v_pk_add_f32 v[24:25], v[28:29], 1.0 op_sel_hi:[1,0]
	v_med3_f32 v23, v23, s54, v206
	v_rcp_f32_e32 v24, v24
	v_rcp_f32_e32 v25, v25
	v_pk_fma_f32 v[30:31], v[112:113], s[18:19], v[0:1] op_sel_hi:[1,0,1]
	v_pk_mul_f32 v[18:19], v[18:19], v[22:23]
	v_pk_fma_f32 v[22:23], v[118:119], s[18:19], v[6:7] op_sel_hi:[1,0,1]
	v_pk_mul_f32 v[18:19], v[18:19], v[24:25]
	v_pk_fma_f32 v[24:25], v[116:117], s[18:19], v[4:5] op_sel_hi:[1,0,1]
	v_med3_f32 v30, v30, s54, v206
	v_min_f32_e32 v24, 0x40e00000, v24
	v_min_f32_e32 v25, 0x40e00000, v25
	v_pk_mul_f32 v[28:29], v[24:25], s[20:21] op_sel_hi:[1,0]
	v_med3_f32 v31, v31, s54, v206
	v_exp_f32_e32 v28, v28
	v_exp_f32_e32 v29, v29
	v_min_f32_e32 v22, 0x40e00000, v22
	v_min_f32_e32 v23, 0x40e00000, v23
	v_pk_add_f32 v[28:29], v[28:29], 1.0 op_sel_hi:[1,0]
	v_pk_mul_f32 v[24:25], v[24:25], v[30:31]
	v_pk_mul_f32 v[30:31], v[22:23], s[20:21] op_sel_hi:[1,0]
	v_rcp_f32_e32 v28, v28
	v_rcp_f32_e32 v29, v29
	v_exp_f32_e32 v30, v30
	v_exp_f32_e32 v31, v31
	v_pk_fma_f32 v[26:27], v[114:115], s[18:19], v[2:3] op_sel_hi:[1,0,1]
	v_pk_mul_f32 v[24:25], v[24:25], v[28:29]
	v_med3_f32 v26, v26, s54, v206
	v_pk_add_f32 v[28:29], v[30:31], 1.0 op_sel_hi:[1,0]
	v_rcp_f32_e32 v28, v28
	v_rcp_f32_e32 v29, v29
	v_med3_f32 v27, v27, s54, v206
	v_cvt_pk_fp8_f32 v30, v20, v21
	v_cvt_pk_fp8_f32 v31, v24, v25
	v_cvt_pk_fp8_f32 v30, v18, v19 op_sel:[0,0,1]
	v_pk_mul_f32 v[20:21], v[22:23], v[26:27]
	v_add_co_u32_e32 v18, vcc, s38, v16
	v_pk_mul_f32 v[20:21], v[20:21], v[28:29]
	s_nop 0
	v_addc_co_u32_e32 v19, vcc, 0, v17, vcc
	v_cvt_pk_fp8_f32 v31, v20, v21 op_sel:[0,0,1]
	global_store_dwordx2 v[18:19], v[30:31], off
	v_pk_fma_f32 v[20:21], v[108:109], s[18:19], v[12:13] op_sel_hi:[1,0,1]
	v_pk_fma_f32 v[18:19], v[110:111], s[18:19], v[14:15] op_sel_hi:[1,0,1]
	v_min_f32_e32 v20, 0x40e00000, v20
	v_min_f32_e32 v21, 0x40e00000, v21
	v_pk_mul_f32 v[24:25], v[20:21], s[20:21] op_sel_hi:[1,0]
	v_min_f32_e32 v18, 0x40e00000, v18
	v_exp_f32_e32 v24, v24
	v_exp_f32_e32 v25, v25
	v_min_f32_e32 v19, 0x40e00000, v19
	v_pk_mul_f32 v[28:29], v[18:19], s[20:21] op_sel_hi:[1,0]
	v_pk_fma_f32 v[26:27], v[104:105], s[18:19], v[8:9] op_sel_hi:[1,0,1]
	v_pk_add_f32 v[24:25], v[24:25], 1.0 op_sel_hi:[1,0]
	v_exp_f32_e32 v28, v28
	v_rcp_f32_e32 v24, v24
	v_rcp_f32_e32 v25, v25
	v_exp_f32_e32 v29, v29
	v_med3_f32 v26, v26, s54, v206
	v_med3_f32 v27, v27, s54, v206
	v_pk_fma_f32 v[22:23], v[106:107], s[18:19], v[10:11] op_sel_hi:[1,0,1]
	v_pk_mul_f32 v[20:21], v[20:21], v[26:27]
	v_med3_f32 v22, v22, s54, v206
	v_pk_mul_f32 v[20:21], v[20:21], v[24:25]
	v_pk_add_f32 v[24:25], v[28:29], 1.0 op_sel_hi:[1,0]
	v_med3_f32 v23, v23, s54, v206
	v_rcp_f32_e32 v24, v24
	v_rcp_f32_e32 v25, v25
	v_pk_fma_f32 v[30:31], v[96:97], s[18:19], v[0:1] op_sel_hi:[1,0,1]
	v_pk_mul_f32 v[18:19], v[18:19], v[22:23]
	v_pk_fma_f32 v[22:23], v[102:103], s[18:19], v[6:7] op_sel_hi:[1,0,1]
	v_pk_mul_f32 v[18:19], v[18:19], v[24:25]
	v_pk_fma_f32 v[24:25], v[100:101], s[18:19], v[4:5] op_sel_hi:[1,0,1]
	v_med3_f32 v30, v30, s54, v206
	v_min_f32_e32 v24, 0x40e00000, v24
	v_min_f32_e32 v25, 0x40e00000, v25
	v_pk_mul_f32 v[28:29], v[24:25], s[20:21] op_sel_hi:[1,0]
	v_med3_f32 v31, v31, s54, v206
	v_exp_f32_e32 v28, v28
	v_exp_f32_e32 v29, v29
	v_min_f32_e32 v22, 0x40e00000, v22
	v_min_f32_e32 v23, 0x40e00000, v23
	v_pk_add_f32 v[28:29], v[28:29], 1.0 op_sel_hi:[1,0]
	v_pk_mul_f32 v[24:25], v[24:25], v[30:31]
	v_pk_mul_f32 v[30:31], v[22:23], s[20:21] op_sel_hi:[1,0]
	v_rcp_f32_e32 v28, v28
	v_rcp_f32_e32 v29, v29
	v_exp_f32_e32 v30, v30
	v_exp_f32_e32 v31, v31
	v_pk_fma_f32 v[26:27], v[98:99], s[18:19], v[2:3] op_sel_hi:[1,0,1]
	v_pk_mul_f32 v[24:25], v[24:25], v[28:29]
	v_med3_f32 v26, v26, s54, v206
	v_pk_add_f32 v[28:29], v[30:31], 1.0 op_sel_hi:[1,0]
	v_rcp_f32_e32 v28, v28
	v_rcp_f32_e32 v29, v29
	v_med3_f32 v27, v27, s54, v206
	v_cvt_pk_fp8_f32 v30, v20, v21
	v_cvt_pk_fp8_f32 v31, v24, v25
	v_cvt_pk_fp8_f32 v30, v18, v19 op_sel:[0,0,1]
	v_pk_mul_f32 v[20:21], v[22:23], v[26:27]
	v_add_co_u32_e32 v18, vcc, s55, v16
	v_pk_mul_f32 v[20:21], v[20:21], v[28:29]
	s_nop 0
	v_addc_co_u32_e32 v19, vcc, 0, v17, vcc
	v_cvt_pk_fp8_f32 v31, v20, v21 op_sel:[0,0,1]
; #define LAS __attribute__((address_space(3)))
; #define PG8_BAR __builtin_amdgcn_s_barrier()
;     ...
;         if (!has_next) break;
; #pragma unroll
;         for (int a = 0; a < 2; ++a)
; #pragma unroll
;             for (int b = 0; b < 2; ++b)
; #pragma unroll
;                 for (int m = 0; m < 4; ++m)
; #pragma unroll
;                     for (int n = 0; n < 2; ++n) acc[a][b][m][n] = (f32x4){0.f, 0.f, 0.f, 0.f};
;         cur = nxt; cA = nA; cB = nB; ++ui;
;         if constexpr (ALIGN_EPI) { if (wr == 1) PG8_BAR; }
;     __device__ __forceinline__ void operator()(const f32x4 (&acc)[2][2][4][2], const Unit& u, int wr, int wc, int fr, int fq) const {
;         unsigned char* base = (unsigned char*)u.O; const int acol = u.a1 * 128 + wc * 32 + 8 * fq;
;         const LAS float* bt = (const LAS float*)((LAS unsigned char*)lds_raw + LDS_CTL_OFF + 4096 + u.buf * 1024) + wc * 32 + 8 * fq;
;         const int row0 = wr * 64 + fr;
;         f32x4 bgv[2], buv[2];
; #pragma unroll
;         for (int n = 0; n < 2; ++n) { bgv[n] = *(const LAS f32x4*)(bt + 4 * n); buv[n] = *(const LAS f32x4*)(bt + 128 + 4 * n); }
; #pragma unroll
;         for (int ai = 0; ai < 2; ++ai)
; #pragma unroll
;             for (int m = 0; m < 4; ++m) {
;                 float o[8];
; #pragma unroll
;                 for (int n = 0; n < 2; ++n) { const f32x4 g4 = acc[ai][0][m][n] * WSCALE_INV + bgv[n], u4 = acc[ai][1][m][n] * WSCALE_INV + buv[n];
; #pragma unroll
;                     for (int e = 0; e < 4; e += 2) {
;                         f32x2 g = {fminf(g4[e], 7.0f), fminf(g4[e + 1], 7.0f)}; const f32x2 up = {fminf(fmaxf(u4[e], -7.0f), 7.0f), fminf(fmaxf(u4[e + 1], -7.0f), 7.0f)};
;                         const f32x2 z = g * (-2.4554669595930157f); f32x2 ex; ex.x = __builtin_amdgcn_exp2f(z.x); ex.y = __builtin_amdgcn_exp2f(z.y);
;                         const f32x2 den = ex + 1.0f; f32x2 sg; sg.x = __builtin_amdgcn_rcpf(den.x); sg.y = __builtin_amdgcn_rcpf(den.y);
;                         const f32x2 r = (up + 1.0f) * g * sg; o[4 * n + e] = r.x; o[4 * n + e + 1] = r.y; } }
;                 u32x2 w; w.x = pk4f8(o[0], o[1], o[2], o[3]); w.y = pk4f8(o[4], o[5], o[6], o[7]);
;                 *(u32x2*)(base + (size_t)(row0 + ai * HALF + m * 16) * 2048 + acol) = w; __builtin_amdgcn_sched_barrier(0); }
	global_store_dwordx2 v[18:19], v[30:31], off
	v_pk_fma_f32 v[20:21], v[92:93], s[18:19], v[12:13] op_sel_hi:[1,0,1]
	v_pk_fma_f32 v[18:19], v[94:95], s[18:19], v[14:15] op_sel_hi:[1,0,1]
	v_min_f32_e32 v20, 0x40e00000, v20
	v_min_f32_e32 v21, 0x40e00000, v21
	v_pk_mul_f32 v[24:25], v[20:21], s[20:21] op_sel_hi:[1,0]
	v_min_f32_e32 v18, 0x40e00000, v18
	v_exp_f32_e32 v24, v24
	v_exp_f32_e32 v25, v25
	v_min_f32_e32 v19, 0x40e00000, v19
	v_pk_mul_f32 v[28:29], v[18:19], s[20:21] op_sel_hi:[1,0]
	v_pk_fma_f32 v[26:27], v[88:89], s[18:19], v[8:9] op_sel_hi:[1,0,1]
	v_pk_add_f32 v[24:25], v[24:25], 1.0 op_sel_hi:[1,0]
	v_exp_f32_e32 v28, v28
	v_rcp_f32_e32 v24, v24
	v_rcp_f32_e32 v25, v25
	v_exp_f32_e32 v29, v29
	v_med3_f32 v26, v26, s54, v206
	v_med3_f32 v27, v27, s54, v206
	v_pk_fma_f32 v[22:23], v[90:91], s[18:19], v[10:11] op_sel_hi:[1,0,1]
	v_pk_mul_f32 v[20:21], v[20:21], v[26:27]
	v_med3_f32 v22, v22, s54, v206
	v_pk_mul_f32 v[20:21], v[20:21], v[24:25]
	v_pk_add_f32 v[24:25], v[28:29], 1.0 op_sel_hi:[1,0]
	v_med3_f32 v23, v23, s54, v206
	v_rcp_f32_e32 v24, v24
	v_rcp_f32_e32 v25, v25
	v_pk_fma_f32 v[30:31], v[80:81], s[18:19], v[0:1] op_sel_hi:[1,0,1]
	v_pk_mul_f32 v[18:19], v[18:19], v[22:23]
	v_pk_fma_f32 v[22:23], v[86:87], s[18:19], v[6:7] op_sel_hi:[1,0,1]
	v_pk_mul_f32 v[18:19], v[18:19], v[24:25]
	v_pk_fma_f32 v[24:25], v[84:85], s[18:19], v[4:5] op_sel_hi:[1,0,1]
	v_med3_f32 v30, v30, s54, v206
	v_min_f32_e32 v24, 0x40e00000, v24
	v_min_f32_e32 v25, 0x40e00000, v25
	v_pk_mul_f32 v[28:29], v[24:25], s[20:21] op_sel_hi:[1,0]
	v_med3_f32 v31, v31, s54, v206
	v_exp_f32_e32 v28, v28
	v_exp_f32_e32 v29, v29
	v_min_f32_e32 v22, 0x40e00000, v22
	v_min_f32_e32 v23, 0x40e00000, v23
	v_pk_add_f32 v[28:29], v[28:29], 1.0 op_sel_hi:[1,0]
	v_pk_mul_f32 v[24:25], v[24:25], v[30:31]
	v_pk_mul_f32 v[30:31], v[22:23], s[20:21] op_sel_hi:[1,0]
	v_rcp_f32_e32 v28, v28
	v_rcp_f32_e32 v29, v29
	v_exp_f32_e32 v30, v30
	v_exp_f32_e32 v31, v31
	v_pk_fma_f32 v[26:27], v[82:83], s[18:19], v[2:3] op_sel_hi:[1,0,1]
	v_pk_mul_f32 v[24:25], v[24:25], v[28:29]
	v_med3_f32 v26, v26, s54, v206
	v_pk_add_f32 v[28:29], v[30:31], 1.0 op_sel_hi:[1,0]
	v_rcp_f32_e32 v28, v28
	v_rcp_f32_e32 v29, v29
	v_med3_f32 v27, v27, s54, v206
	v_cvt_pk_fp8_f32 v30, v20, v21
	v_cvt_pk_fp8_f32 v31, v24, v25
	v_cvt_pk_fp8_f32 v30, v18, v19 op_sel:[0,0,1]
	v_pk_mul_f32 v[20:21], v[22:23], v[26:27]
	v_add_co_u32_e32 v18, vcc, s56, v16
	v_pk_mul_f32 v[20:21], v[20:21], v[28:29]
	s_nop 0
	v_addc_co_u32_e32 v19, vcc, 0, v17, vcc
	v_cvt_pk_fp8_f32 v31, v20, v21 op_sel:[0,0,1]
	global_store_dwordx2 v[18:19], v[30:31], off
	v_pk_fma_f32 v[14:15], v[78:79], s[18:19], v[14:15] op_sel_hi:[1,0,1]
	v_pk_fma_f32 v[8:9], v[72:73], s[18:19], v[8:9] op_sel_hi:[1,0,1]
	v_min_f32_e32 v14, 0x40e00000, v14
	v_min_f32_e32 v15, 0x40e00000, v15
	v_pk_mul_f32 v[20:21], v[14:15], s[20:21] op_sel_hi:[1,0]
	v_pk_fma_f32 v[12:13], v[76:77], s[18:19], v[12:13] op_sel_hi:[1,0,1]
	v_exp_f32_e32 v20, v20
	v_exp_f32_e32 v21, v21
	v_med3_f32 v8, v8, s54, v206
	v_med3_f32 v9, v9, s54, v206
	v_min_f32_e32 v12, 0x40e00000, v12
	v_min_f32_e32 v13, 0x40e00000, v13
	v_pk_mul_f32 v[18:19], v[12:13], s[20:21] op_sel_hi:[1,0]
	v_pk_mul_f32 v[8:9], v[12:13], v[8:9]
	v_pk_add_f32 v[12:13], v[20:21], 1.0 op_sel_hi:[1,0]
	v_pk_fma_f32 v[10:11], v[74:75], s[18:19], v[10:11] op_sel_hi:[1,0,1]
	v_rcp_f32_e32 v12, v12
	v_rcp_f32_e32 v13, v13
	v_med3_f32 v10, v10, s54, v206
	v_med3_f32 v11, v11, s54, v206
	v_pk_fma_f32 v[4:5], v[68:69], s[18:19], v[4:5] op_sel_hi:[1,0,1]
	v_pk_mul_f32 v[10:11], v[14:15], v[10:11]
	v_min_f32_e32 v4, 0x40e00000, v4
	v_min_f32_e32 v5, 0x40e00000, v5
	v_pk_mul_f32 v[10:11], v[10:11], v[12:13]
	v_pk_mul_f32 v[12:13], v[4:5], s[20:21] op_sel_hi:[1,0]
	v_pk_fma_f32 v[0:1], v[64:65], s[18:19], v[0:1] op_sel_hi:[1,0,1]
	v_exp_f32_e32 v18, v18
	v_exp_f32_e32 v19, v19
	v_exp_f32_e32 v12, v12
	v_exp_f32_e32 v13, v13
	v_med3_f32 v0, v0, s54, v206
	v_med3_f32 v1, v1, s54, v206
	v_pk_fma_f32 v[6:7], v[70:71], s[18:19], v[6:7] op_sel_hi:[1,0,1]
	v_pk_add_f32 v[18:19], v[18:19], 1.0 op_sel_hi:[1,0]
	v_pk_mul_f32 v[0:1], v[4:5], v[0:1]
	v_min_f32_e32 v4, 0x40e00000, v6
	v_min_f32_e32 v5, 0x40e00000, v7
	v_pk_mul_f32 v[6:7], v[4:5], s[20:21] op_sel_hi:[1,0]
	v_pk_add_f32 v[12:13], v[12:13], 1.0 op_sel_hi:[1,0]
	v_exp_f32_e32 v6, v6
	v_exp_f32_e32 v7, v7
	v_rcp_f32_e32 v18, v18
	v_rcp_f32_e32 v19, v19
	v_rcp_f32_e32 v12, v12
	v_rcp_f32_e32 v13, v13
	v_pk_add_f32 v[6:7], v[6:7], 1.0 op_sel_hi:[1,0]
	v_pk_mul_f32 v[8:9], v[8:9], v[18:19]
	v_pk_fma_f32 v[2:3], v[66:67], s[18:19], v[2:3] op_sel_hi:[1,0,1]
	v_pk_mul_f32 v[0:1], v[0:1], v[12:13]
	v_rcp_f32_e32 v6, v6
	v_rcp_f32_e32 v7, v7
	v_med3_f32 v2, v2, s54, v206
	v_med3_f32 v3, v3, s54, v206
	v_cvt_pk_fp8_f32 v12, v8, v9
	v_cvt_pk_fp8_f32 v13, v0, v1
	v_cvt_pk_fp8_f32 v12, v10, v11 op_sel:[0,0,1]
	v_pk_mul_f32 v[0:1], v[4:5], v[2:3]
	s_nop 0
	v_pk_mul_f32 v[0:1], v[0:1], v[6:7]
	s_nop 0
	v_cvt_pk_fp8_f32 v13, v0, v1 op_sel:[0,0,1]
	v_add_co_u32_e32 v0, vcc, 0x58000, v16
	s_nop 1
	v_addc_co_u32_e32 v1, vcc, 0, v17, vcc
	global_store_dwordx2 v[0:1], v[12:13], off
	s_and_b64 vcc, exec, s[0:1]
	s_mov_b64 s[0:1], -1
	s_cbranch_vccnz .LBB0_1229
	s_andn2_b64 vcc, exec, s[14:15]
	s_cbranch_vccnz .LBB0_1228
	s_barrier
	s_branch .LBB0_1228
